# proj: epilogue bias loads hoisted into first K-loop iteration (counted vmcnt), epilogue vmcnt(0) drain removed
# baseline (speedup 1.0000x reference)
.LBB4_22:
	s_add_u32 s34, s26, s30
	s_addc_u32 s35, s27, s31
	s_add_u32 s34, s34, 0x180
	s_addc_u32 s35, s35, 0
	s_add_u32 s68, s28, s30
	s_addc_u32 s69, s29, s31
	s_add_u32 s70, s68, 0x180
	s_addc_u32 s71, s69, 0
	s_cmp_eq_u32 s60, s67
	s_cselect_b32 s69, s5, s35
	s_cselect_b32 s68, s4, s34
	s_cselect_b32 s35, s7, s71
	s_cselect_b32 s34, s6, s70
	s_add_i32 s70, s62, s44
	v_lshl_add_u64 v[108:109], v[98:99], 0, s[30:31]
	s_mov_b32 m0, s70
	ds_read_b128 v[130:133], v136 offset:16384
	ds_read_b128 v[142:145], v136 offset:17408
	ds_read_b128 v[146:149], v136 offset:18432
	ds_read_b128 v[150:153], v136 offset:19456
	ds_read_b128 v[154:157], v137
	ds_read_b128 v[158:161], v137 offset:1024
	ds_read_b128 v[162:165], v137 offset:2048
	ds_read_b128 v[166:169], v137 offset:3072
	ds_read_b128 v[170:173], v137 offset:4096
	ds_read_b128 v[174:177], v137 offset:5120
	ds_read_b128 v[178:181], v137 offset:6144
	ds_read_b128 v[182:185], v137 offset:7168
	global_load_lds_dwordx4 v[108:109], off
	v_lshl_add_u64 v[108:109], v[100:101], 0, s[30:31]
	s_add_i32 m0, s70, 0x2000
	s_nop 0
	global_load_lds_dwordx4 v[108:109], off
	s_barrier
	s_waitcnt lgkmcnt(0)
	s_setprio 1
	s_waitcnt lgkmcnt(0)
	v_mfma_f32_16x16x32_f16 v[94:97], v[130:133], v[154:157], v[94:97]
	v_mfma_f32_16x16x32_f16 v[90:93], v[146:149], v[154:157], v[90:93]
	v_mfma_f32_16x16x32_f16 v[82:85], v[130:133], v[162:165], v[82:85]
	v_mfma_f32_16x16x32_f16 v[78:81], v[146:149], v[162:165], v[78:81]
	v_mfma_f32_16x16x32_f16 v[70:73], v[130:133], v[170:173], v[70:73]
	v_mfma_f32_16x16x32_f16 v[66:69], v[146:149], v[170:173], v[66:69]
	v_mfma_f32_16x16x32_f16 v[58:61], v[130:133], v[178:181], v[58:61]
	v_mfma_f32_16x16x32_f16 v[54:57], v[146:149], v[178:181], v[54:57]
	v_mfma_f32_16x16x32_f16 v[94:97], v[142:145], v[158:161], v[94:97]
	v_mfma_f32_16x16x32_f16 v[90:93], v[150:153], v[158:161], v[90:93]
	v_mfma_f32_16x16x32_f16 v[82:85], v[142:145], v[166:169], v[82:85]
	v_mfma_f32_16x16x32_f16 v[78:81], v[150:153], v[166:169], v[78:81]
	v_mfma_f32_16x16x32_f16 v[70:73], v[142:145], v[174:177], v[70:73]
	v_mfma_f32_16x16x32_f16 v[66:69], v[150:153], v[174:177], v[66:69]
	v_mfma_f32_16x16x32_f16 v[58:61], v[142:145], v[182:185], v[58:61]
	v_mfma_f32_16x16x32_f16 v[54:57], v[150:153], v[182:185], v[54:57]
	s_setprio 0
	s_barrier
	v_lshl_add_u64 v[108:109], v[102:103], 0, s[30:31]
	s_add_i32 m0, s49, 0x18000
	ds_read_b128 v[130:133], v136 offset:20480
	ds_read_b128 v[142:145], v136 offset:21504
	global_load_lds_dwordx4 v[108:109], off
	v_lshl_add_u64 v[108:109], v[104:105], 0, s[30:31]
	s_add_i32 m0, s49, 0x1a000
	s_nop 0
	global_load_lds_dwordx4 v[108:109], off
	v_lshl_add_u64 v[108:109], v[106:107], 0, s[30:31]
	s_add_i32 m0, s49, 0x1c000
	s_nop 0
	global_load_lds_dwordx4 v[108:109], off
	s_cmp_lg_u32 s67, 0
	s_cbranch_scc1 .Lpj_norm_0
	s_mul_i32 s72, s66, 0xc0
	v_add_u32_e32 v214, s72, v135
	v_ashrrev_i32_e32 v215, 31, v214
	v_lshl_add_u64 v[214:215], v[214:215], 2, s[10:11]
	global_load_dwordx4 v[202:205], v[214:215], off
	global_load_dwordx4 v[206:209], v[214:215], off offset:64
	global_load_dwordx4 v[210:213], v[214:215], off offset:128
	global_load_dwordx4 v[2:5], v[194:195], off
	global_load_dwordx4 v[6:9], v[194:195], off offset:64
	global_load_dwordx4 v[10:13], v[194:195], off offset:128
	global_load_dwordx4 v[14:17], v[196:197], off
	s_waitcnt vmcnt(12)
	s_branch .Lpj_join_0

.Lpj_join_0:
	s_barrier
	s_waitcnt lgkmcnt(0)
	s_setprio 1
	s_waitcnt lgkmcnt(0)
	v_mfma_f32_16x16x32_f16 v[86:89], v[130:133], v[154:157], v[86:89]
	v_mfma_f32_16x16x32_f16 v[74:77], v[130:133], v[162:165], v[74:77]
	v_mfma_f32_16x16x32_f16 v[62:65], v[130:133], v[170:173], v[62:65]
	v_mfma_f32_16x16x32_f16 v[50:53], v[130:133], v[178:181], v[50:53]
	v_mfma_f32_16x16x32_f16 v[86:89], v[142:145], v[158:161], v[86:89]
	v_mfma_f32_16x16x32_f16 v[74:77], v[142:145], v[166:169], v[74:77]
	v_mfma_f32_16x16x32_f16 v[62:65], v[142:145], v[174:177], v[62:65]
	v_mfma_f32_16x16x32_f16 v[50:53], v[142:145], v[182:185], v[50:53]
	s_setprio 0
	s_barrier
	s_mov_b32 m0, s49
	v_lshl_add_u64 v[108:109], s[68:69], 0, v[110:111]
	ds_read_b128 v[130:133], v136 offset:57344
	ds_read_b128 v[142:145], v136 offset:58368
	ds_read_b128 v[146:149], v136 offset:59392
	ds_read_b128 v[150:153], v136 offset:60416
	ds_read_b128 v[154:157], v137 offset:40960
	ds_read_b128 v[158:161], v137 offset:41984
	ds_read_b128 v[162:165], v137 offset:43008
	ds_read_b128 v[166:169], v137 offset:44032
	ds_read_b128 v[170:173], v137 offset:45056
	ds_read_b128 v[174:177], v137 offset:46080
	ds_read_b128 v[178:181], v137 offset:47104
	ds_read_b128 v[182:185], v137 offset:48128
	global_load_lds_dwordx4 v[108:109], off
	v_lshl_add_u64 v[186:187], s[68:69], 0, v[114:115]
	s_mov_b32 m0, s50
	s_nop 0
	global_load_lds_dwordx4 v[186:187], off
	s_barrier
	s_waitcnt lgkmcnt(0)
	s_setprio 1
	s_waitcnt lgkmcnt(0)
	v_mfma_f32_16x16x32_f16 v[94:97], v[130:133], v[154:157], v[94:97]
	v_mfma_f32_16x16x32_f16 v[90:93], v[146:149], v[154:157], v[90:93]
	v_mfma_f32_16x16x32_f16 v[82:85], v[130:133], v[162:165], v[82:85]
	v_mfma_f32_16x16x32_f16 v[78:81], v[146:149], v[162:165], v[78:81]
	v_mfma_f32_16x16x32_f16 v[70:73], v[130:133], v[170:173], v[70:73]
	v_mfma_f32_16x16x32_f16 v[66:69], v[146:149], v[170:173], v[66:69]
	v_mfma_f32_16x16x32_f16 v[58:61], v[130:133], v[178:181], v[58:61]
	v_mfma_f32_16x16x32_f16 v[54:57], v[146:149], v[178:181], v[54:57]
	v_mfma_f32_16x16x32_f16 v[94:97], v[142:145], v[158:161], v[94:97]
	v_mfma_f32_16x16x32_f16 v[90:93], v[150:153], v[158:161], v[90:93]
	v_mfma_f32_16x16x32_f16 v[82:85], v[142:145], v[166:169], v[82:85]
	v_mfma_f32_16x16x32_f16 v[78:81], v[150:153], v[166:169], v[78:81]
	v_mfma_f32_16x16x32_f16 v[70:73], v[142:145], v[174:177], v[70:73]
	v_mfma_f32_16x16x32_f16 v[66:69], v[150:153], v[174:177], v[66:69]
	v_mfma_f32_16x16x32_f16 v[58:61], v[142:145], v[182:185], v[58:61]
	v_mfma_f32_16x16x32_f16 v[54:57], v[150:153], v[182:185], v[54:57]
	s_setprio 0
	s_barrier
	s_mov_b32 m0, s51
	v_lshl_add_u64 v[188:189], s[34:35], 0, v[112:113]
	ds_read_b128 v[130:133], v136 offset:61440
	ds_read_b128 v[142:145], v136 offset:62464
	global_load_lds_dwordx4 v[188:189], off
	v_lshl_add_u64 v[190:191], s[34:35], 0, v[116:117]
	s_mov_b32 m0, s52
	v_lshl_add_u64 v[192:193], s[34:35], 0, v[118:119]
	global_load_lds_dwordx4 v[190:191], off
	s_mov_b32 m0, s53
	s_nop 0
	global_load_lds_dwordx4 v[192:193], off
	s_cmp_lg_u32 s67, 0
	s_cbranch_scc1 .Lpj_norm_1
	global_load_dwordx4 v[18:21], v[196:197], off offset:64
	global_load_dwordx4 v[22:25], v[196:197], off offset:128
	global_load_dwordx4 v[26:29], v[198:199], off
	global_load_dwordx4 v[30:33], v[198:199], off offset:64
	s_waitcnt vmcnt(16)
	s_branch .Lpj_join_1

.LBB4_23:
	s_mul_i32 s26, s66, 0xc0
	v_add_u32_e32 v132, s26, v135
	v_ashrrev_i32_e32 v133, 31, v132
	v_lshl_add_u64 v[98:99], v[132:133], 2, s[10:11]
	v_and_b32_e32 v130, 64, v140
	v_xor_b32_e32 v131, 16, v140
	v_add_u32_e32 v142, 64, v130
	v_cmp_lt_i32_e32 vcc, v131, v142
	v_xor_b32_e32 v141, 32, v140
	v_lshl_add_u32 v143, s65, 7, v134
	v_cndmask_b32_e32 v131, v140, v131, vcc
	v_cmp_lt_i32_e32 vcc, v141, v142
	v_lshlrev_b32_e32 v142, 2, v131
	v_mad_i64_i32 v[144:145], s[26:27], v143, s41, 0
	v_lshl_add_u64 v[144:145], v[144:145], 1, s[12:13]
	v_cndmask_b32_e32 v141, v140, v141, vcc
	v_lshl_add_u64 v[144:145], v[132:133], 1, v[144:145]
	v_lshlrev_b32_e32 v141, 2, v141
	v_lshlrev_b32_e32 v130, 1, v143
	v_pk_add_f32 v[96:97], v[96:97], v[204:205]
	v_pk_add_f32 v[94:95], v[94:95], v[202:203]
	v_pk_add_f32 v[92:93], v[92:93], v[208:209]
	v_pk_add_f32 v[90:91], v[90:91], v[206:207]
	v_pk_add_f32 v[88:89], v[88:89], v[212:213]
	v_pk_add_f32 v[86:87], v[86:87], v[210:211]
	v_pk_add_f32 v[96:97], v[4:5], v[96:97]
	v_pk_add_f32 v[94:95], v[2:3], v[94:95]
	v_pk_add_f32 v[92:93], v[8:9], v[92:93]
	v_pk_add_f32 v[90:91], v[6:7], v[90:91]
	v_pk_add_f32 v[146:147], v[12:13], v[88:89]
	v_pk_add_f32 v[148:149], v[10:11], v[86:87]
	v_cvt_pk_f16_f32 v86, v94, v95
	v_cvt_pk_f16_f32 v87, v96, v97
	v_add_f32_e32 v89, v94, v95
	v_add_f32_e32 v131, v96, v97
	v_mul_f32_e32 v95, v95, v95
	v_mul_f32_e32 v97, v97, v97
	v_cvt_pk_f16_f32 v88, v90, v91
	v_add_f32_e32 v150, v90, v91
	v_mul_f32_e32 v91, v91, v91
	v_mul_f32_e32 v152, v93, v93
	v_add_f32_e32 v151, v92, v93
	v_mul_f32_e32 v155, v149, v149
	v_mul_f32_e32 v156, v147, v147
	v_add_f32_e32 v89, v89, v131
	v_fmac_f32_e32 v95, v94, v94
	v_fmac_f32_e32 v97, v96, v96
	v_fmac_f32_e32 v91, v90, v90
	v_fmac_f32_e32 v152, v92, v92
	v_add_f32_e32 v153, v148, v149
	v_add_f32_e32 v154, v146, v147
	v_add_f32_e32 v94, v150, v151
	v_fmac_f32_e32 v155, v148, v148
	v_fmac_f32_e32 v156, v146, v146
	v_add_f32_e32 v89, 0, v89
	v_add_f32_e32 v95, v95, v97
	v_add_f32_e32 v91, v91, v152
	v_add_f32_e32 v90, v153, v154
	v_add_f32_e32 v96, v155, v156
	v_add_f32_e32 v89, v89, v94
	v_add_f32_e32 v91, v95, v91
	v_add_f32_e32 v90, v89, v90
	v_add_f32_e32 v91, v91, v96
	ds_bpermute_b32 v94, v142, v90
	ds_bpermute_b32 v95, v142, v91
	v_cvt_pk_f16_f32 v89, v92, v93
	global_store_dwordx2 v[144:145], v[86:87], off
	global_store_dwordx2 v[144:145], v[88:89], off offset:32
	v_ashrrev_i32_e32 v131, 31, v130
	s_waitcnt lgkmcnt(1)
	v_add_f32_e32 v86, v90, v94
	s_waitcnt lgkmcnt(0)
	v_add_f32_e32 v87, v91, v95
	ds_bpermute_b32 v88, v141, v86
	ds_bpermute_b32 v89, v141, v87
	v_cvt_pk_f16_f32 v90, v148, v149
	v_cvt_pk_f16_f32 v91, v146, v147
	global_store_dwordx2 v[144:145], v[90:91], off offset:64
	s_and_saveexec_b64 s[26:27], s[0:1]
	s_cbranch_execz .LBB4_25
	v_lshl_add_u64 v[90:91], v[130:131], 2, s[14:15]
	s_waitcnt lgkmcnt(1)
	v_add_f32_e32 v86, v86, v88
	s_waitcnt lgkmcnt(0)
	v_add_f32_e32 v87, v87, v89
	global_atomic_add_f32 v[90:91], v86, off
	global_atomic_add_f32 v[90:91], v87, off offset:4
.LBB4_25:
	s_or_b64 exec, exec, s[26:27]
	s_waitcnt lgkmcnt(1)
	v_or_b32_e32 v88, 16, v143
	v_pk_add_f32 v[84:85], v[84:85], v[204:205]
	v_pk_add_f32 v[82:83], v[82:83], v[202:203]
	s_waitcnt lgkmcnt(0)
	v_mad_i64_i32 v[88:89], s[26:27], v88, s41, 0
	v_pk_add_f32 v[84:85], v[16:17], v[84:85]
	v_pk_add_f32 v[82:83], v[14:15], v[82:83]
	v_lshl_add_u64 v[88:89], v[88:89], 1, s[12:13]
	v_cvt_pk_f16_f32 v86, v82, v83
	v_cvt_pk_f16_f32 v87, v84, v85
	v_lshl_add_u64 v[88:89], v[132:133], 1, v[88:89]
	global_store_dwordx2 v[88:89], v[86:87], off
	v_add_f32_e32 v86, v82, v83
	v_mul_f32_e32 v83, v83, v83
	v_fmac_f32_e32 v83, v82, v82
	v_mul_f32_e32 v82, v85, v85
	v_pk_add_f32 v[80:81], v[80:81], v[208:209]
	v_pk_add_f32 v[78:79], v[78:79], v[206:207]
	v_add_f32_e32 v87, v84, v85
	v_fmac_f32_e32 v82, v84, v84
	v_pk_add_f32 v[80:81], v[20:21], v[80:81]
	v_pk_add_f32 v[78:79], v[18:19], v[78:79]
	v_add_f32_e32 v86, v86, v87
	v_add_f32_e32 v82, v83, v82
	v_add_f32_e32 v83, v78, v79
	v_add_f32_e32 v84, v80, v81
	v_add_f32_e32 v86, 0, v86
	v_add_f32_e32 v83, v83, v84
	v_add_f32_e32 v86, v86, v83
	v_mul_f32_e32 v83, v79, v79
	v_mul_f32_e32 v84, v81, v81
	v_fmac_f32_e32 v83, v78, v78
	v_fmac_f32_e32 v84, v80, v80
	v_add_f32_e32 v83, v83, v84
	v_pk_add_f32 v[76:77], v[76:77], v[212:213]
	v_pk_add_f32 v[74:75], v[74:75], v[210:211]
	v_add_f32_e32 v87, v82, v83
	v_pk_add_f32 v[82:83], v[24:25], v[76:77]
	v_pk_add_f32 v[84:85], v[22:23], v[74:75]
	v_add_f32_e32 v75, v82, v83
	v_add_f32_e32 v74, v84, v85
	v_add_f32_e32 v74, v74, v75
	v_mul_f32_e32 v75, v85, v85
	v_mul_f32_e32 v76, v83, v83
	v_fmac_f32_e32 v75, v84, v84
	v_fmac_f32_e32 v76, v82, v82
	v_add_f32_e32 v75, v75, v76
	v_add_f32_e32 v74, v86, v74
	v_add_f32_e32 v77, v87, v75
	ds_bpermute_b32 v76, v142, v74
	ds_bpermute_b32 v86, v142, v77
	v_cvt_pk_f16_f32 v78, v78, v79
	v_cvt_pk_f16_f32 v79, v80, v81
	global_store_dwordx2 v[88:89], v[78:79], off offset:32
	s_waitcnt lgkmcnt(1)
	v_add_f32_e32 v74, v74, v76
	s_waitcnt lgkmcnt(0)
	v_add_f32_e32 v76, v77, v86
	ds_bpermute_b32 v75, v141, v74
	ds_bpermute_b32 v77, v141, v76
	v_cvt_pk_f16_f32 v78, v84, v85
	v_cvt_pk_f16_f32 v79, v82, v83
	global_store_dwordx2 v[88:89], v[78:79], off offset:64
	s_and_saveexec_b64 s[26:27], s[0:1]
	s_cbranch_execz .LBB4_27
	v_lshl_add_u64 v[78:79], v[130:131], 2, s[14:15]
	s_waitcnt lgkmcnt(1)
	v_add_f32_e32 v74, v74, v75
	s_waitcnt lgkmcnt(0)
	v_add_f32_e32 v75, v76, v77
	global_atomic_add_f32 v[78:79], v74, off offset:128
	global_atomic_add_f32 v[78:79], v75, off offset:132
.LBB4_27:
	s_or_b64 exec, exec, s[26:27]
	v_or_b32_e32 v76, 32, v143
	v_pk_add_f32 v[72:73], v[72:73], v[204:205]
	v_pk_add_f32 v[70:71], v[70:71], v[202:203]
	s_waitcnt lgkmcnt(0)
	v_mad_i64_i32 v[76:77], s[26:27], v76, s41, 0
	v_pk_add_f32 v[72:73], v[28:29], v[72:73]
	v_pk_add_f32 v[70:71], v[26:27], v[70:71]
	v_lshl_add_u64 v[76:77], v[76:77], 1, s[12:13]
	v_cvt_pk_f16_f32 v74, v70, v71
	v_cvt_pk_f16_f32 v75, v72, v73
	v_lshl_add_u64 v[76:77], v[132:133], 1, v[76:77]
	global_store_dwordx2 v[76:77], v[74:75], off
	v_add_f32_e32 v74, v70, v71
	v_mul_f32_e32 v71, v71, v71
	v_fmac_f32_e32 v71, v70, v70
	v_mul_f32_e32 v70, v73, v73
	v_pk_add_f32 v[68:69], v[68:69], v[208:209]
	v_pk_add_f32 v[66:67], v[66:67], v[206:207]
	v_add_f32_e32 v75, v72, v73
	v_fmac_f32_e32 v70, v72, v72
	v_pk_add_f32 v[68:69], v[32:33], v[68:69]
	v_pk_add_f32 v[66:67], v[30:31], v[66:67]
	v_add_f32_e32 v74, v74, v75
	v_add_f32_e32 v70, v71, v70
	v_add_f32_e32 v71, v66, v67
	v_add_f32_e32 v72, v68, v69
	v_add_f32_e32 v74, 0, v74
	v_add_f32_e32 v71, v71, v72
	v_add_f32_e32 v74, v74, v71
	v_mul_f32_e32 v71, v67, v67
	v_mul_f32_e32 v72, v69, v69
	v_fmac_f32_e32 v71, v66, v66
	v_fmac_f32_e32 v72, v68, v68
	v_add_f32_e32 v71, v71, v72
	v_pk_add_f32 v[64:65], v[64:65], v[212:213]
	v_pk_add_f32 v[62:63], v[62:63], v[210:211]
	v_add_f32_e32 v75, v70, v71
	v_pk_add_f32 v[70:71], v[36:37], v[64:65]
	v_pk_add_f32 v[72:73], v[34:35], v[62:63]
	v_add_f32_e32 v63, v70, v71
	v_add_f32_e32 v62, v72, v73
	v_add_f32_e32 v62, v62, v63
	v_mul_f32_e32 v63, v73, v73
	v_mul_f32_e32 v64, v71, v71
	v_fmac_f32_e32 v63, v72, v72
	v_fmac_f32_e32 v64, v70, v70
	v_add_f32_e32 v63, v63, v64
	v_add_f32_e32 v62, v74, v62
	v_add_f32_e32 v65, v75, v63
	ds_bpermute_b32 v64, v142, v62
	ds_bpermute_b32 v74, v142, v65
	v_cvt_pk_f16_f32 v66, v66, v67
	v_cvt_pk_f16_f32 v67, v68, v69
	global_store_dwordx2 v[76:77], v[66:67], off offset:32
	s_waitcnt lgkmcnt(1)
	v_add_f32_e32 v62, v62, v64
	s_waitcnt lgkmcnt(0)
	v_add_f32_e32 v64, v65, v74
	ds_bpermute_b32 v63, v141, v62
	ds_bpermute_b32 v65, v141, v64
	v_cvt_pk_f16_f32 v66, v72, v73
	v_cvt_pk_f16_f32 v67, v70, v71
	global_store_dwordx2 v[76:77], v[66:67], off offset:64
	s_and_saveexec_b64 s[26:27], s[0:1]
	s_cbranch_execz .LBB4_29
	v_lshl_add_u64 v[66:67], v[130:131], 2, s[14:15]
	s_waitcnt lgkmcnt(1)
	v_add_f32_e32 v62, v62, v63
	s_waitcnt lgkmcnt(0)
	v_add_f32_e32 v63, v64, v65
	global_atomic_add_f32 v[66:67], v62, off offset:256
	global_atomic_add_f32 v[66:67], v63, off offset:260
.LBB4_29:
	s_or_b64 exec, exec, s[26:27]
	v_or_b32_e32 v64, 48, v143
	v_pk_add_f32 v[60:61], v[60:61], v[204:205]
	v_pk_add_f32 v[58:59], v[58:59], v[202:203]
	s_waitcnt lgkmcnt(0)
	v_mad_i64_i32 v[64:65], s[26:27], v64, s41, 0
	v_pk_add_f32 v[60:61], v[40:41], v[60:61]
	v_pk_add_f32 v[58:59], v[38:39], v[58:59]
	v_lshl_add_u64 v[64:65], v[64:65], 1, s[12:13]
	v_cvt_pk_f16_f32 v62, v58, v59
	v_cvt_pk_f16_f32 v63, v60, v61
	v_lshl_add_u64 v[64:65], v[132:133], 1, v[64:65]
	global_store_dwordx2 v[64:65], v[62:63], off
	v_add_f32_e32 v62, v58, v59
	v_mul_f32_e32 v59, v59, v59
	v_fmac_f32_e32 v59, v58, v58
	v_mul_f32_e32 v58, v61, v61
	v_pk_add_f32 v[56:57], v[56:57], v[208:209]
	v_pk_add_f32 v[54:55], v[54:55], v[206:207]
	v_add_f32_e32 v63, v60, v61
	v_fmac_f32_e32 v58, v60, v60
	v_pk_add_f32 v[56:57], v[44:45], v[56:57]
	v_pk_add_f32 v[54:55], v[42:43], v[54:55]
	v_add_f32_e32 v62, v62, v63
	v_add_f32_e32 v58, v59, v58
	v_add_f32_e32 v59, v54, v55
	v_add_f32_e32 v60, v56, v57
	v_add_f32_e32 v62, 0, v62
	v_add_f32_e32 v59, v59, v60
	v_add_f32_e32 v62, v62, v59
	v_mul_f32_e32 v59, v55, v55
	v_mul_f32_e32 v60, v57, v57
	v_fmac_f32_e32 v59, v54, v54
	v_fmac_f32_e32 v60, v56, v56
	v_add_f32_e32 v59, v59, v60
	v_pk_add_f32 v[52:53], v[52:53], v[212:213]
	v_pk_add_f32 v[50:51], v[50:51], v[210:211]
	v_add_f32_e32 v63, v58, v59
	v_pk_add_f32 v[58:59], v[48:49], v[52:53]
	v_pk_add_f32 v[60:61], v[46:47], v[50:51]
	v_add_f32_e32 v51, v58, v59
	v_add_f32_e32 v50, v60, v61
	v_add_f32_e32 v50, v50, v51
	v_mul_f32_e32 v51, v61, v61
	v_mul_f32_e32 v52, v59, v59
	v_fmac_f32_e32 v51, v60, v60
	v_fmac_f32_e32 v52, v58, v58
	v_add_f32_e32 v51, v51, v52
	v_add_f32_e32 v50, v62, v50
	v_add_f32_e32 v53, v63, v51
	ds_bpermute_b32 v52, v142, v50
	ds_bpermute_b32 v62, v142, v53
	v_cvt_pk_f16_f32 v54, v54, v55
	v_cvt_pk_f16_f32 v55, v56, v57
	global_store_dwordx2 v[64:65], v[54:55], off offset:32
	s_waitcnt lgkmcnt(1)
	v_add_f32_e32 v50, v50, v52
	s_waitcnt lgkmcnt(0)
	v_add_f32_e32 v52, v53, v62
	ds_bpermute_b32 v51, v141, v50
	ds_bpermute_b32 v53, v141, v52
	v_cvt_pk_f16_f32 v54, v60, v61
	v_cvt_pk_f16_f32 v55, v58, v59
	global_store_dwordx2 v[64:65], v[54:55], off offset:64
	s_and_saveexec_b64 s[26:27], s[0:1]
	s_cbranch_execz .LBB4_9
	v_lshl_add_u64 v[54:55], v[130:131], 2, s[14:15]
	s_waitcnt lgkmcnt(1)
	v_add_f32_e32 v50, v50, v51
	s_waitcnt lgkmcnt(0)
	v_add_f32_e32 v51, v52, v53
	global_atomic_add_f32 v[54:55], v50, off offset:384
	global_atomic_add_f32 v[54:55], v51, off offset:388
	s_branch .LBB4_9

	.amdhsa_kernel _Z9k_gemm192IN4g19210EpiResStatEEvNS0_4GemmET_
		.amdhsa_group_segment_fixed_size 0
		.amdhsa_private_segment_fixed_size 0
		.amdhsa_kernarg_size 344
		.amdhsa_user_sgpr_count 2
		.amdhsa_user_sgpr_dispatch_ptr 0
		.amdhsa_user_sgpr_queue_ptr 0
		.amdhsa_user_sgpr_kernarg_segment_ptr 1
		.amdhsa_user_sgpr_dispatch_id 0
		.amdhsa_user_sgpr_kernarg_preload_length 0
		.amdhsa_user_sgpr_kernarg_preload_offset 0
		.amdhsa_user_sgpr_private_segment_size 0
		.amdhsa_uses_dynamic_stack 0
		.amdhsa_enable_private_segment 0
		.amdhsa_system_sgpr_workgroup_id_x 1
		.amdhsa_system_sgpr_workgroup_id_y 0
		.amdhsa_system_sgpr_workgroup_id_z 0
		.amdhsa_system_sgpr_workgroup_info 0
		.amdhsa_system_vgpr_workitem_id 0
		.amdhsa_next_free_vgpr 216
		.amdhsa_next_free_sgpr 74
		.amdhsa_accum_offset 216
		.amdhsa_reserve_vcc 1
		.amdhsa_float_round_mode_32 0
		.amdhsa_float_round_mode_16_64 0
		.amdhsa_float_denorm_mode_32 3
		.amdhsa_float_denorm_mode_16_64 3
		.amdhsa_dx10_clamp 1
		.amdhsa_ieee_mode 1
		.amdhsa_fp16_overflow 0
		.amdhsa_tg_split 0
		.amdhsa_exception_fp_ieee_invalid_op 0
		.amdhsa_exception_fp_denorm_src 0
		.amdhsa_exception_fp_ieee_div_zero 0
		.amdhsa_exception_fp_ieee_overflow 0
		.amdhsa_exception_fp_ieee_underflow 0
		.amdhsa_exception_fp_ieee_inexact 0
		.amdhsa_exception_int_div_zero 0
	.end_amdhsa_kernel

amdhsa.kernels:
  - .agpr_count:     0
    .args:
      - .offset:         0
        .size:           224
        .value_kind:     by_value
      - .actual_access:  read_only
        .address_space:  global
        .offset:         224
        .size:           8
        .value_kind:     global_buffer
      - .actual_access:  read_only
        .address_space:  global
        .offset:         232
        .size:           8
        .value_kind:     global_buffer
      - .actual_access:  read_only
        .address_space:  global
        .offset:         240
        .size:           8
        .value_kind:     global_buffer
      - .actual_access:  write_only
        .address_space:  global
        .offset:         248
        .size:           8
        .value_kind:     global_buffer
      - .offset:         256
        .size:           4
        .value_kind:     hidden_block_count_x
      - .offset:         260
        .size:           4
        .value_kind:     hidden_block_count_y
      - .offset:         264
        .size:           4
        .value_kind:     hidden_block_count_z
      - .offset:         268
        .size:           2
        .value_kind:     hidden_group_size_x
      - .offset:         270
        .size:           2
        .value_kind:     hidden_group_size_y
      - .offset:         272
        .size:           2
        .value_kind:     hidden_group_size_z
      - .offset:         274
        .size:           2
        .value_kind:     hidden_remainder_x
      - .offset:         276
        .size:           2
        .value_kind:     hidden_remainder_y
      - .offset:         278
        .size:           2
        .value_kind:     hidden_remainder_z
      - .offset:         296
        .size:           8
        .value_kind:     hidden_global_offset_x
      - .offset:         304
        .size:           8
        .value_kind:     hidden_global_offset_y
      - .offset:         312
        .size:           8
        .value_kind:     hidden_global_offset_z
      - .offset:         320
        .size:           2
        .value_kind:     hidden_grid_dims
    .group_segment_fixed_size: 16640
    .kernarg_segment_align: 8
    .kernarg_segment_size: 512
    .language:       OpenCL C
    .language_version:
      - 2
      - 0
    .max_flat_workgroup_size: 256
    .name:           _Z10k_prep_ln18PrepArgsPKfS1_S1_Pt
    .private_segment_fixed_size: 0
    .sgpr_count:     28
    .sgpr_spill_count: 0
    .symbol:         _Z10k_prep_ln18PrepArgsPKfS1_S1_Pt.kd
    .uniform_work_group_size: 1
    .uses_dynamic_stack: false
    .vgpr_count:     75
    .vgpr_spill_count: 0
    .wavefront_size: 64
  - .agpr_count:     0
    .args:
      - .actual_access:  read_only
        .address_space:  global
        .offset:         0
        .size:           8
        .value_kind:     global_buffer
      - .actual_access:  read_only
        .address_space:  global
        .offset:         8
        .size:           8
        .value_kind:     global_buffer
      - .actual_access:  read_only
        .address_space:  global
        .offset:         16
        .size:           8
        .value_kind:     global_buffer
      - .actual_access:  write_only
        .address_space:  global
        .offset:         24
        .size:           8
        .value_kind:     global_buffer
    .group_segment_fixed_size: 0
    .kernarg_segment_align: 8
    .kernarg_segment_size: 32
    .language:       OpenCL C
    .language_version:
      - 2
      - 0
    .max_flat_workgroup_size: 256
    .name:           _Z5k_ln2PKfS0_S0_Pt
    .private_segment_fixed_size: 0
    .sgpr_count:     18
    .sgpr_spill_count: 0
    .symbol:         _Z5k_ln2PKfS0_S0_Pt.kd
    .uniform_work_group_size: 1
    .uses_dynamic_stack: false
    .vgpr_count:     54
    .vgpr_spill_count: 0
    .wavefront_size: 64
  - .agpr_count:     0
    .args:
      - .actual_access:  read_only
        .address_space:  global
        .offset:         0
        .size:           8
        .value_kind:     global_buffer
      - .actual_access:  read_only
        .address_space:  global
        .offset:         8
        .size:           8
        .value_kind:     global_buffer
      - .actual_access:  read_only
        .address_space:  global
        .offset:         16
        .size:           8
        .value_kind:     global_buffer
      - .actual_access:  read_only
        .address_space:  global
        .offset:         24
        .size:           8
        .value_kind:     global_buffer
      - .actual_access:  read_only
        .address_space:  global
        .offset:         32
        .size:           8
        .value_kind:     global_buffer
      - .actual_access:  write_only
        .address_space:  global
        .offset:         40
        .size:           8
        .value_kind:     global_buffer
      - .offset:         48
        .size:           224
        .value_kind:     by_value
    .group_segment_fixed_size: 0
    .kernarg_segment_align: 8
    .kernarg_segment_size: 272
    .language:       OpenCL C
    .language_version:
      - 2
      - 0
    .max_flat_workgroup_size: 256
    .name:           _Z6k_attnPKtS0_S0_S0_S0_Pt8PrepArgs
    .private_segment_fixed_size: 0
    .sgpr_count:     30
    .sgpr_spill_count: 0
    .symbol:         _Z6k_attnPKtS0_S0_S0_S0_Pt8PrepArgs.kd
    .uniform_work_group_size: 1
    .uses_dynamic_stack: false
    .vgpr_count:     244
    .vgpr_spill_count: 0
    .wavefront_size: 64
  - .agpr_count:     0
    .args:
      - .offset:         0
        .size:           40
        .value_kind:     by_value
      - .offset:         40
        .size:           32
        .value_kind:     by_value
      - .offset:         72
        .size:           4
        .value_kind:     hidden_block_count_x
      - .offset:         76
        .size:           4
        .value_kind:     hidden_block_count_y
      - .offset:         80
        .size:           4
        .value_kind:     hidden_block_count_z
      - .offset:         84
        .size:           2
        .value_kind:     hidden_group_size_x
      - .offset:         86
        .size:           2
        .value_kind:     hidden_group_size_y
      - .offset:         88
        .size:           2
        .value_kind:     hidden_group_size_z
      - .offset:         90
        .size:           2
        .value_kind:     hidden_remainder_x
      - .offset:         92
        .size:           2
        .value_kind:     hidden_remainder_y
      - .offset:         94
        .size:           2
        .value_kind:     hidden_remainder_z
      - .offset:         112
        .size:           8
        .value_kind:     hidden_global_offset_x
      - .offset:         120
        .size:           8
        .value_kind:     hidden_global_offset_y
      - .offset:         128
        .size:           8
        .value_kind:     hidden_global_offset_z
      - .offset:         136
        .size:           2
        .value_kind:     hidden_grid_dims
      - .offset:         192
        .size:           4
        .value_kind:     hidden_dynamic_lds_size
    .group_segment_fixed_size: 0
    .kernarg_segment_align: 8
    .kernarg_segment_size: 328
    .language:       OpenCL C
    .language_version:
      - 2
      - 0
    .max_flat_workgroup_size: 512
    .name:           _Z9k_gemm192IN4g1926EpiQKVEEvNS0_4GemmET_
    .private_segment_fixed_size: 0
    .sgpr_count:     74
    .sgpr_spill_count: 0
    .symbol:         _Z9k_gemm192IN4g1926EpiQKVEEvNS0_4GemmET_.kd
    .uniform_work_group_size: 1
    .uses_dynamic_stack: false
    .vgpr_count:     156
    .vgpr_spill_count: 0
    .wavefront_size: 64
  - .agpr_count:     0
    .args:
      - .offset:         0
        .size:           40
        .value_kind:     by_value
      - .offset:         40
        .size:           48
        .value_kind:     by_value
      - .offset:         88
        .size:           4
        .value_kind:     hidden_block_count_x
      - .offset:         92
        .size:           4
        .value_kind:     hidden_block_count_y
      - .offset:         96
        .size:           4
        .value_kind:     hidden_block_count_z
      - .offset:         100
        .size:           2
        .value_kind:     hidden_group_size_x
      - .offset:         102
        .size:           2
        .value_kind:     hidden_group_size_y
      - .offset:         104
        .size:           2
        .value_kind:     hidden_group_size_z
      - .offset:         106
        .size:           2
        .value_kind:     hidden_remainder_x
      - .offset:         108
        .size:           2
        .value_kind:     hidden_remainder_y
      - .offset:         110
        .size:           2
        .value_kind:     hidden_remainder_z
      - .offset:         128
        .size:           8
        .value_kind:     hidden_global_offset_x
      - .offset:         136
        .size:           8
        .value_kind:     hidden_global_offset_y
      - .offset:         144
        .size:           8
        .value_kind:     hidden_global_offset_z
      - .offset:         152
        .size:           2
        .value_kind:     hidden_grid_dims
      - .offset:         208
        .size:           4
        .value_kind:     hidden_dynamic_lds_size
    .group_segment_fixed_size: 0
    .kernarg_segment_align: 8
    .kernarg_segment_size: 344
    .language:       OpenCL C
    .language_version:
      - 2
      - 0
    .max_flat_workgroup_size: 512
    .name:           _Z9k_gemm192IN4g19210EpiResStatEEvNS0_4GemmET_
    .private_segment_fixed_size: 0
    .sgpr_count:     78
    .sgpr_spill_count: 0
    .symbol:         _Z9k_gemm192IN4g19210EpiResStatEEvNS0_4GemmET_.kd
    .uniform_work_group_size: 1
    .uses_dynamic_stack: false
    .vgpr_count:     216
    .vgpr_spill_count: 0
    .wavefront_size: 64
  - .agpr_count:     0
    .args:
      - .offset:         0
        .size:           40
        .value_kind:     by_value
      - .offset:         40
        .size:           48
        .value_kind:     by_value
      - .offset:         88
        .size:           4
        .value_kind:     hidden_block_count_x
      - .offset:         92
        .size:           4
        .value_kind:     hidden_block_count_y
      - .offset:         96
        .size:           4
        .value_kind:     hidden_block_count_z
      - .offset:         100
        .size:           2
        .value_kind:     hidden_group_size_x
      - .offset:         102
        .size:           2
        .value_kind:     hidden_group_size_y
      - .offset:         104
        .size:           2
        .value_kind:     hidden_group_size_z
      - .offset:         106
        .size:           2
        .value_kind:     hidden_remainder_x
      - .offset:         108
        .size:           2
        .value_kind:     hidden_remainder_y
      - .offset:         110
        .size:           2
        .value_kind:     hidden_remainder_z
      - .offset:         128
        .size:           8
        .value_kind:     hidden_global_offset_x
      - .offset:         136
        .size:           8
        .value_kind:     hidden_global_offset_y
      - .offset:         144
        .size:           8
        .value_kind:     hidden_global_offset_z
      - .offset:         152
        .size:           2
        .value_kind:     hidden_grid_dims
      - .offset:         208
        .size:           4
        .value_kind:     hidden_dynamic_lds_size
    .group_segment_fixed_size: 0
    .kernarg_segment_align: 8
    .kernarg_segment_size: 344
    .language:       OpenCL C
    .language_version:
      - 2
      - 0
    .max_flat_workgroup_size: 512
    .name:           _Z9k_gemm128IN4g1289EpiGeluLNEEvNS0_4GemmET_
    .private_segment_fixed_size: 0
    .sgpr_count:     84
    .sgpr_spill_count: 0
    .symbol:         _Z9k_gemm128IN4g1289EpiGeluLNEEvNS0_4GemmET_.kd
    .uniform_work_group_size: 1
    .uses_dynamic_stack: false
    .vgpr_count:     170
    .vgpr_spill_count: 0
    .wavefront_size: 64
  - .agpr_count:     0
    .args:
      - .offset:         0
        .size:           40
        .value_kind:     by_value
      - .offset:         40
        .size:           32
        .value_kind:     by_value
      - .offset:         72
        .size:           4
        .value_kind:     hidden_block_count_x
      - .offset:         76
        .size:           4
        .value_kind:     hidden_block_count_y
      - .offset:         80
        .size:           4
        .value_kind:     hidden_block_count_z
      - .offset:         84
        .size:           2
        .value_kind:     hidden_group_size_x
      - .offset:         86
        .size:           2
        .value_kind:     hidden_group_size_y
      - .offset:         88
        .size:           2
        .value_kind:     hidden_group_size_z
      - .offset:         90
        .size:           2
        .value_kind:     hidden_remainder_x
      - .offset:         92
        .size:           2
        .value_kind:     hidden_remainder_y
      - .offset:         94
        .size:           2
        .value_kind:     hidden_remainder_z
      - .offset:         112
        .size:           8
        .value_kind:     hidden_global_offset_x
      - .offset:         120
        .size:           8
        .value_kind:     hidden_global_offset_y
      - .offset:         128
        .size:           8
        .value_kind:     hidden_global_offset_z
      - .offset:         136
        .size:           2
        .value_kind:     hidden_grid_dims
      - .offset:         192
        .size:           4
        .value_kind:     hidden_dynamic_lds_size
    .group_segment_fixed_size: 0
    .kernarg_segment_align: 8
    .kernarg_segment_size: 328
    .language:       OpenCL C
    .language_version:
      - 2
      - 0
    .max_flat_workgroup_size: 512
    .name:           _Z9k_gemm192IN4g1927EpiResHEEvNS0_4GemmET_
    .private_segment_fixed_size: 0
    .sgpr_count:     76
    .sgpr_spill_count: 0
    .symbol:         _Z9k_gemm192IN4g1927EpiResHEEvNS0_4GemmET_.kd
    .uniform_work_group_size: 1
    .uses_dynamic_stack: false
    .vgpr_count:     190
    .vgpr_spill_count: 0
    .wavefront_size: 64
